# prologue weight transposes: all sixteen row loads of an item issued up front, LDS writes behind counted waits
# speedup vs baseline: 1.0077x; 1.0077x over previous
.LBB0_24:
	s_mov_b32 s0, 0x38e38e39
	v_mul_hi_i32 v46, v45, s0
	v_lshrrev_b32_e32 v47, 31, v46
	v_ashrrev_i32_e32 v46, 3, v46
	v_add_u32_e32 v46, v46, v47
	s_movk_i32 s0, 0xf700
	v_lshlrev_b32_e32 v54, 6, v46
	v_mad_u64_u32 v[46:47], s[0:1], v46, s0, v[12:13]
	v_add_u32_e32 v48, 0x600, v46
	v_or_b32_e32 v60, v54, v1
	v_ashrrev_i32_e32 v49, 31, v48
	s_movk_i32 s0, 0x280
	v_or_b32_e32 v50, 4, v60
	v_lshl_add_u64 v[56:57], v[48:49], 2, v[8:9]
	v_add_u32_e32 v74, v46, v3
	v_cmp_gt_u32_e32 vcc, s0, v46
	v_add_u32_e32 v75, v46, v5
	v_mad_i64_i32 v[46:47], s[0:1], v60, s19, v[56:57]
	v_mad_i64_i32 v[50:51], s[0:1], v50, s19, v[56:57]
	global_load_dwordx4 v[162:165], v[46:47], off nt
	s_nop 0
	global_load_dwordx4 v[166:169], v[50:51], off nt
	v_or_b32_e32 v58, 8, v60
	v_or_b32_e32 v59, 12, v60
	v_or_b32_e32 v61, 16, v60
	v_ashrrev_i32_e32 v55, 31, v54
	v_or_b32_e32 v64, 20, v60
	v_lshl_add_u64 v[62:63], v[54:55], 1, v[10:11]
	v_mad_i64_i32 v[54:55], s[0:1], v64, s19, v[56:57]
	v_or_b32_e32 v65, 24, v60
	v_or_b32_e32 v66, 28, v60
	v_or_b32_e32 v67, 32, v60
	v_or_b32_e32 v68, 36, v60
	v_or_b32_e32 v69, 40, v60
	v_or_b32_e32 v70, 44, v60
	v_or_b32_e32 v71, 48, v60
	v_or_b32_e32 v72, 52, v60
	v_or_b32_e32 v73, 56, v60
	v_or_b32_e32 v76, 60, v60
	v_add_u32_e32 v77, 0x600, v74
	v_add_u32_e32 v78, 0x600, v75
	v_add_u32_e32 v45, s22, v45
	v_add_u32_e32 v12, s18, v12
	v_mad_i64_i32 v[46:47], s[0:1], v58, s19, v[56:57]
	v_mad_i64_i32 v[58:59], s[0:1], v59, s19, v[56:57]
	global_load_dwordx4 v[170:173], v[46:47], off nt
	s_nop 0
	global_load_dwordx4 v[174:177], v[58:59], off nt
	v_mad_i64_i32 v[58:59], s[4:5], v67, s19, v[56:57]
	v_mad_i64_i32 v[46:47], s[0:1], v61, s19, v[56:57]
	global_load_dwordx4 v[178:181], v[46:47], off nt
	s_nop 0
	global_load_dwordx4 v[182:185], v[54:55], off nt
	v_mad_i64_i32 v[54:55], s[4:5], v66, s19, v[56:57]
	v_mad_i64_i32 v[60:61], s[4:5], v69, s19, v[56:57]
	v_mad_i64_i32 v[66:67], s[4:5], v71, s19, v[56:57]
	v_cmp_gt_i32_e64 s[0:1], s20, v77
	s_or_b64 s[0:1], s[0:1], vcc
	v_mad_i64_i32 v[46:47], s[4:5], v65, s19, v[56:57]
	global_load_dwordx4 v[186:189], v[46:47], off nt
	s_nop 0
	global_load_dwordx4 v[190:193], v[54:55], off nt
	v_mad_i64_i32 v[54:55], s[4:5], v68, s19, v[56:57]
	v_mad_i64_i32 v[64:65], s[4:5], v70, s19, v[56:57]
	v_mad_i64_i32 v[68:69], s[4:5], v73, s19, v[56:57]
	v_mad_i64_i32 v[70:71], s[4:5], v76, s19, v[56:57]
	global_load_dwordx4 v[194:197], v[58:59], off nt
	global_load_dwordx4 v[198:201], v[54:55], off nt
	v_mad_i64_i32 v[58:59], s[4:5], v72, s19, v[56:57]
	v_cndmask_b32_e64 v72, v77, v78, s[0:1]
	v_ashrrev_i32_e32 v73, 31, v72
	global_load_dwordx4 v[202:205], v[60:61], off nt
	global_load_dwordx4 v[206:209], v[64:65], off nt
	global_load_dwordx4 v[210:213], v[66:67], off nt
	v_lshlrev_b64 v[64:65], 11, v[72:73]
	v_lshl_add_u64 v[64:65], v[62:63], 0, v[64:65]
	v_add_u32_e32 v72, 0x620, v74
	global_load_dwordx4 v[214:217], v[58:59], off nt
	s_nop 0
	global_load_dwordx4 v[218:221], v[68:69], off nt
	global_load_dwordx4 v[222:225], v[70:71], off nt
	s_waitcnt vmcnt(15)
	ds_write2_b32 v14, v162, v163 offset1:1
	ds_write2_b32 v14, v164, v165 offset0:2 offset1:3
	s_waitcnt vmcnt(14)
	ds_write2_b32 v7, v166, v167 offset1:1
	ds_write2_b32 v15, v168, v169 offset1:1
	s_waitcnt vmcnt(13)
	ds_write2_b32 v16, v170, v171 offset1:1
	ds_write2_b32 v17, v172, v173 offset1:1
	s_waitcnt vmcnt(12)
	ds_write2_b32 v18, v174, v175 offset1:1
	ds_write2_b32 v19, v176, v177 offset1:1
	s_waitcnt vmcnt(11)
	ds_write2_b32 v20, v178, v179 offset1:1
	ds_write2_b32 v21, v180, v181 offset1:1
	s_waitcnt vmcnt(10)
	ds_write2_b32 v22, v182, v183 offset1:1
	ds_write2_b32 v23, v184, v185 offset1:1
	s_waitcnt vmcnt(9)
	ds_write2_b32 v24, v186, v187 offset1:1
	ds_write2_b32 v25, v188, v189 offset1:1
	s_waitcnt vmcnt(8)
	ds_write2_b32 v26, v190, v191 offset1:1
	ds_write2_b32 v27, v192, v193 offset1:1
	s_waitcnt vmcnt(7)
	ds_write2_b32 v28, v194, v195 offset1:1
	ds_write2_b32 v29, v196, v197 offset1:1
	s_waitcnt vmcnt(6)
	ds_write2_b32 v30, v198, v199 offset1:1
	ds_write2_b32 v31, v200, v201 offset1:1
	s_waitcnt vmcnt(5)
	ds_write2_b32 v32, v202, v203 offset1:1
	ds_write2_b32 v33, v204, v205 offset1:1
	s_waitcnt vmcnt(4)
	ds_write2_b32 v34, v206, v207 offset1:1
	ds_write2_b32 v35, v208, v209 offset1:1
	s_waitcnt vmcnt(3)
	ds_write2_b32 v36, v210, v211 offset1:1
	ds_write2_b32 v37, v212, v213 offset1:1
	s_waitcnt vmcnt(2)
	ds_write2_b32 v38, v214, v215 offset1:1
	ds_write2_b32 v39, v216, v217 offset1:1
	s_waitcnt vmcnt(1)
	ds_write2_b32 v40, v218, v219 offset1:1
	ds_write2_b32 v41, v220, v221 offset1:1
	s_waitcnt vmcnt(0)
	ds_write2_b32 v42, v222, v223 offset1:1
	ds_write2_b32 v43, v224, v225 offset1:1
	s_waitcnt lgkmcnt(0)
	ds_read2_b32 v[50:51], v13 offset0:65 offset1:73
	ds_read2_b32 v[52:53], v13 offset1:8
	ds_read2_b32 v[54:55], v13 offset0:130 offset1:138
	ds_read2_b32 v[56:57], v13 offset0:195 offset1:203
	ds_read2_b32 v[58:59], v44 offset0:4 offset1:12
	ds_read2_b32 v[60:61], v44 offset0:69 offset1:77
	ds_read2_b32 v[66:67], v44 offset0:134 offset1:142
	ds_read2_b32 v[68:69], v44 offset0:199 offset1:207
	s_waitcnt lgkmcnt(6)
	v_cvt_pk_bf16_f32 v46, v52, v50
	s_waitcnt lgkmcnt(4)
	v_cvt_pk_bf16_f32 v47, v54, v56
	s_waitcnt lgkmcnt(2)
	v_cvt_pk_bf16_f32 v48, v58, v60
	s_waitcnt lgkmcnt(0)
	v_cvt_pk_bf16_f32 v49, v66, v68
	global_store_dwordx4 v[64:65], v[46:49], off
	s_nop 1
	v_add_u32_e32 v46, 0x608, v74
	v_add_u32_e32 v48, 0x610, v74
	v_cmp_gt_i32_e64 s[0:1], s20, v46
	v_add_u32_e32 v47, 0x610, v75
	v_cmp_gt_i32_e64 s[4:5], s20, v48
	s_or_b64 s[0:1], s[0:1], vcc
	v_add_u32_e32 v49, 0x620, v75
	v_cndmask_b32_e64 v46, v46, v47, s[0:1]
	s_or_b64 s[0:1], s[4:5], vcc
	v_cndmask_b32_e64 v48, v48, v49, s[0:1]
	v_ashrrev_i32_e32 v47, 31, v46
	v_ashrrev_i32_e32 v49, 31, v48
	v_lshlrev_b64 v[46:47], 11, v[46:47]
	v_lshlrev_b64 v[48:49], 11, v[48:49]
	v_lshl_add_u64 v[64:65], v[62:63], 0, v[46:47]
	v_lshl_add_u64 v[70:71], v[62:63], 0, v[48:49]
	v_cvt_pk_bf16_f32 v46, v53, v51
	v_cvt_pk_bf16_f32 v47, v55, v57
	v_cvt_pk_bf16_f32 v48, v59, v61
	v_cvt_pk_bf16_f32 v49, v67, v69
	ds_read2_b32 v[50:51], v13 offset0:16 offset1:24
	ds_read2_b32 v[52:53], v13 offset0:81 offset1:89
	ds_read2_b32 v[54:55], v13 offset0:146 offset1:154
	ds_read2_b32 v[56:57], v13 offset0:211 offset1:219
	ds_read2_b32 v[58:59], v44 offset0:20 offset1:28
	ds_read2_b32 v[60:61], v44 offset0:85 offset1:93
	global_store_dwordx4 v[64:65], v[46:49], off
	ds_read2_b32 v[64:65], v44 offset0:150 offset1:158
	ds_read2_b32 v[66:67], v44 offset0:215 offset1:223
	s_waitcnt lgkmcnt(6)
	v_cvt_pk_bf16_f32 v46, v50, v52
	s_waitcnt lgkmcnt(4)
	v_cvt_pk_bf16_f32 v47, v54, v56
	s_waitcnt lgkmcnt(2)
	v_cvt_pk_bf16_f32 v48, v58, v60
	s_waitcnt lgkmcnt(0)
	v_cvt_pk_bf16_f32 v49, v64, v66
	global_store_dwordx4 v[70:71], v[46:49], off
	ds_read2_b32 v[70:71], v13 offset0:32 offset1:40
	s_nop 0
	v_add_u32_e32 v46, 0x618, v74
	v_cmp_gt_i32_e64 s[0:1], s20, v46
	v_add_u32_e32 v47, 0x630, v75
	s_or_b64 s[0:1], s[0:1], vcc
	v_cndmask_b32_e64 v46, v46, v47, s[0:1]
	v_ashrrev_i32_e32 v47, 31, v46
	v_lshlrev_b64 v[46:47], 11, v[46:47]
	v_lshl_add_u64 v[68:69], v[62:63], 0, v[46:47]
	v_cvt_pk_bf16_f32 v46, v51, v53
	v_cvt_pk_bf16_f32 v47, v55, v57
	ds_read2_b32 v[50:51], v13 offset0:97 offset1:105
	ds_read2_b32 v[52:53], v13 offset0:162 offset1:170
	ds_read2_b32 v[54:55], v13 offset0:227 offset1:235
	ds_read2_b32 v[56:57], v44 offset0:36 offset1:44
	v_cvt_pk_bf16_f32 v48, v59, v61
	ds_read2_b32 v[58:59], v44 offset0:101 offset1:109
	ds_read2_b32 v[60:61], v44 offset0:166 offset1:174
	v_cvt_pk_bf16_f32 v49, v65, v67
	global_store_dwordx4 v[68:69], v[46:49], off
	ds_read2_b32 v[64:65], v44 offset0:231 offset1:239
	ds_read2_b32 v[66:67], v13 offset0:48 offset1:56
	ds_read2_b32 v[68:69], v13 offset0:113 offset1:121
	s_waitcnt lgkmcnt(6)
	v_cvt_pk_bf16_f32 v47, v52, v54
	s_waitcnt lgkmcnt(4)
	v_cvt_pk_bf16_f32 v48, v56, v58
	v_cvt_pk_bf16_f32 v52, v57, v59
	ds_read2_b32 v[56:57], v13 offset0:178 offset1:186
	ds_read2_b32 v[58:59], v13 offset0:243 offset1:251
	v_cvt_pk_bf16_f32 v46, v70, v50
	v_cvt_pk_bf16_f32 v50, v71, v51
	v_cvt_pk_bf16_f32 v51, v53, v55
	s_waitcnt lgkmcnt(4)
	v_cvt_pk_bf16_f32 v49, v60, v64
	v_cvt_pk_bf16_f32 v53, v61, v65
	s_waitcnt lgkmcnt(2)
	v_cvt_pk_bf16_f32 v54, v66, v68
	s_waitcnt lgkmcnt(0)
	v_cvt_pk_bf16_f32 v55, v56, v58
	v_cvt_pk_bf16_f32 v58, v67, v69
	v_cvt_pk_bf16_f32 v59, v57, v59
	ds_read2_b32 v[56:57], v44 offset0:52 offset1:60
	ds_read2_b32 v[60:61], v44 offset0:117 offset1:125
	ds_read2_b32 v[64:65], v44 offset0:182 offset1:190
	ds_read2_b32 v[66:67], v44 offset0:247 offset1:255
	v_cmp_gt_i32_e64 s[0:1], s20, v72
	v_add_u32_e32 v69, 0x638, v74
	s_or_b64 s[0:1], s[0:1], vcc
	s_waitcnt lgkmcnt(2)
	v_cvt_pk_bf16_f32 v56, v56, v60
	v_cvt_pk_bf16_f32 v60, v57, v61
	s_waitcnt lgkmcnt(0)
	v_cvt_pk_bf16_f32 v61, v65, v67
	v_add_u32_e32 v65, 0x628, v74
	v_cvt_pk_bf16_f32 v57, v64, v66
	v_add_u32_e32 v64, 0x601, v75
	v_add_u32_e32 v67, 0x630, v74
	v_cmp_gt_i32_e64 s[4:5], s20, v65
	v_add_u32_e32 v66, 0x611, v75
	v_cmp_gt_i32_e64 s[6:7], s20, v67
	v_cmp_gt_i32_e64 s[8:9], s20, v69
	v_cndmask_b32_e64 v64, v72, v64, s[0:1]
	s_or_b64 s[0:1], s[4:5], vcc
	v_add_u32_e32 v68, 0x621, v75
	v_add_u32_e32 v70, 0x631, v75
	v_cndmask_b32_e64 v66, v65, v66, s[0:1]
	s_or_b64 s[0:1], s[6:7], vcc
	s_or_b64 vcc, s[8:9], vcc
	v_cndmask_b32_e64 v68, v67, v68, s[0:1]
	v_cndmask_b32_e32 v70, v69, v70, vcc
	v_ashrrev_i32_e32 v65, 31, v64
	v_ashrrev_i32_e32 v67, 31, v66
	v_ashrrev_i32_e32 v69, 31, v68
	v_ashrrev_i32_e32 v71, 31, v70
	v_lshlrev_b64 v[64:65], 11, v[64:65]
	v_lshlrev_b64 v[66:67], 11, v[66:67]
	v_lshlrev_b64 v[68:69], 11, v[68:69]
	v_lshlrev_b64 v[70:71], 11, v[70:71]
	v_lshl_add_u64 v[64:65], v[62:63], 0, v[64:65]
	v_lshl_add_u64 v[66:67], v[62:63], 0, v[66:67]
	v_lshl_add_u64 v[68:69], v[62:63], 0, v[68:69]
	v_lshl_add_u64 v[62:63], v[62:63], 0, v[70:71]
	global_store_dwordx4 v[64:65], v[46:49], off
	global_store_dwordx4 v[66:67], v[50:53], off
	global_store_dwordx4 v[68:69], v[54:57], off
	global_store_dwordx4 v[62:63], v[58:61], off
	s_waitcnt lgkmcnt(0)
	s_movk_i32 s0, 0x23f
	v_cmp_lt_i32_e32 vcc, s0, v45
	s_or_b64 s[16:17], vcc, s[16:17]
	s_andn2_b64 exec, exec, s[16:17]
	s_cbranch_execnz .LBB0_24

.LBB0_27:
	v_ashrrev_i32_e32 v8, 31, v53
	v_lshrrev_b32_e32 v8, 23, v8
	v_add_u32_e32 v8, v53, v8
	v_ashrrev_i32_e32 v10, 9, v8
	v_mul_i32_i24_e32 v8, 0x200, v10
	v_sub_u32_e32 v54, v53, v8
	v_ashrrev_i16_e32 v55, 15, v54
	v_lshrrev_b16_e32 v55, 11, v55
	v_add_u16_e32 v55, v54, v55
	v_ashrrev_i16_e32 v56, 5, v55
	v_and_b32_e32 v55, 0xffffffe0, v55
	v_ashrrev_i32_e32 v11, 31, v10
	v_sub_u16_e32 v55, v54, v55
	v_lshlrev_b32_sdwa v54, v51, sext(v56) dst_sel:DWORD dst_unused:UNUSED_PAD src0_sel:DWORD src1_sel:WORD_0
	v_lshlrev_b64 v[8:9], 23, v[10:11]
	v_lshlrev_b64 v[10:11], 22, v[10:11]
	v_lshlrev_b32_sdwa v56, v51, sext(v55) dst_sel:DWORD dst_unused:UNUSED_PAD src0_sel:DWORD src1_sel:WORD_0
	v_or_b32_e32 v58, v54, v1
	v_lshl_add_u64 v[8:9], s[22:23], 0, v[8:9]
	v_lshl_add_u64 v[10:11], s[4:5], 0, v[10:11]
	v_ashrrev_i32_e32 v55, 31, v54
	v_ashrrev_i32_e32 v57, 31, v56
	v_or_b32_e32 v60, 4, v58
	v_or_b32_e32 v62, 8, v58
	v_or_b32_e32 v64, 12, v58
	v_or_b32_e32 v66, 16, v58
	v_or_b32_e32 v68, 20, v58
	v_or_b32_e32 v70, 24, v58
	v_or_b32_e32 v72, 28, v58
	v_or_b32_e32 v74, 32, v58
	v_or_b32_e32 v76, 36, v58
	v_ashrrev_i32_e32 v59, 31, v58
	v_or_b32_e32 v78, 40, v58
	v_or_b32_e32 v80, 44, v58
	v_or_b32_e32 v82, 48, v58
	v_or_b32_e32 v84, 52, v58
	v_or_b32_e32 v86, 56, v58
	v_or_b32_e32 v88, 60, v58
	v_lshl_add_u64 v[10:11], v[54:55], 1, v[10:11]
	v_or_b32_e32 v54, v56, v3
	v_or_b32_e32 v90, v56, v12
	v_or_b32_e32 v92, v56, v15
	v_or_b32_e32 v94, v56, v16
	v_or_b32_e32 v96, v56, v17
	v_or_b32_e32 v98, v56, v18
	v_or_b32_e32 v100, v56, v19
	v_or_b32_e32 v102, v56, v20
	v_lshl_add_u64 v[8:9], v[56:57], 2, v[8:9]
	v_ashrrev_i32_e32 v61, 31, v60
	v_ashrrev_i32_e32 v63, 31, v62
	v_ashrrev_i32_e32 v65, 31, v64
	v_ashrrev_i32_e32 v67, 31, v66
	v_ashrrev_i32_e32 v69, 31, v68
	v_ashrrev_i32_e32 v71, 31, v70
	v_ashrrev_i32_e32 v73, 31, v72
	v_ashrrev_i32_e32 v75, 31, v74
	v_ashrrev_i32_e32 v77, 31, v76
	v_lshlrev_b64 v[56:57], 13, v[58:59]
	v_ashrrev_i32_e32 v79, 31, v78
	v_ashrrev_i32_e32 v81, 31, v80
	v_ashrrev_i32_e32 v83, 31, v82
	v_ashrrev_i32_e32 v85, 31, v84
	v_ashrrev_i32_e32 v87, 31, v86
	v_ashrrev_i32_e32 v89, 31, v88
	v_ashrrev_i32_e32 v55, 31, v54
	v_ashrrev_i32_e32 v91, 31, v90
	v_ashrrev_i32_e32 v93, 31, v92
	v_ashrrev_i32_e32 v95, 31, v94
	v_ashrrev_i32_e32 v97, 31, v96
	v_ashrrev_i32_e32 v99, 31, v98
	v_ashrrev_i32_e32 v101, 31, v100
	v_ashrrev_i32_e32 v103, 31, v102
	v_lshl_add_u64 v[8:9], v[8:9], 0, v[4:5]
	v_lshlrev_b64 v[58:59], 13, v[60:61]
	v_lshlrev_b64 v[60:61], 13, v[62:63]
	v_lshlrev_b64 v[62:63], 13, v[64:65]
	v_lshlrev_b64 v[64:65], 13, v[66:67]
	v_lshlrev_b64 v[66:67], 13, v[68:69]
	v_lshlrev_b64 v[68:69], 13, v[70:71]
	v_lshlrev_b64 v[70:71], 13, v[72:73]
	v_lshlrev_b64 v[72:73], 13, v[74:75]
	v_lshlrev_b64 v[74:75], 13, v[76:77]
	v_lshl_add_u64 v[10:11], v[10:11], 0, v[6:7]
	v_lshlrev_b64 v[76:77], 13, v[78:79]
	v_lshlrev_b64 v[78:79], 13, v[80:81]
	v_lshlrev_b64 v[80:81], 13, v[82:83]
	v_lshlrev_b64 v[82:83], 13, v[84:85]
	v_lshlrev_b64 v[84:85], 13, v[86:87]
	v_lshlrev_b64 v[86:87], 13, v[88:89]
	v_lshlrev_b64 v[54:55], 11, v[54:55]
	v_lshlrev_b64 v[88:89], 11, v[90:91]
	v_lshlrev_b64 v[90:91], 11, v[92:93]
	v_lshlrev_b64 v[92:93], 11, v[94:95]
	v_lshlrev_b64 v[94:95], 11, v[96:97]
	v_lshlrev_b64 v[96:97], 11, v[98:99]
	v_lshlrev_b64 v[98:99], 11, v[100:101]
	v_lshlrev_b64 v[100:101], 11, v[102:103]
	v_lshl_add_u64 v[56:57], v[8:9], 0, v[56:57]
	v_lshl_add_u64 v[58:59], v[8:9], 0, v[58:59]
	v_lshl_add_u64 v[60:61], v[8:9], 0, v[60:61]
	v_lshl_add_u64 v[62:63], v[8:9], 0, v[62:63]
	v_lshl_add_u64 v[102:103], v[8:9], 0, v[64:65]
	v_lshl_add_u64 v[104:105], v[8:9], 0, v[66:67]
	v_lshl_add_u64 v[106:107], v[8:9], 0, v[68:69]
	v_lshl_add_u64 v[108:109], v[8:9], 0, v[70:71]
	v_lshl_add_u64 v[110:111], v[8:9], 0, v[72:73]
	v_lshl_add_u64 v[112:113], v[8:9], 0, v[74:75]
	v_lshl_add_u64 v[114:115], v[8:9], 0, v[76:77]
	v_lshl_add_u64 v[116:117], v[8:9], 0, v[78:79]
	v_lshl_add_u64 v[118:119], v[8:9], 0, v[80:81]
	v_lshl_add_u64 v[120:121], v[8:9], 0, v[82:83]
	v_lshl_add_u64 v[122:123], v[8:9], 0, v[84:85]
	v_lshl_add_u64 v[124:125], v[8:9], 0, v[86:87]
	v_lshl_add_u64 v[126:127], v[10:11], 0, v[54:55]
	v_lshl_add_u64 v[128:129], v[10:11], 0, v[88:89]
	v_lshl_add_u64 v[132:133], v[10:11], 0, v[90:91]
	v_lshl_add_u64 v[134:135], v[10:11], 0, v[92:93]
	v_lshl_add_u64 v[136:137], v[10:11], 0, v[94:95]
	v_lshl_add_u64 v[138:139], v[10:11], 0, v[96:97]
	v_lshl_add_u64 v[140:141], v[10:11], 0, v[98:99]
	v_lshl_add_u64 v[142:143], v[10:11], 0, v[100:101]
	global_load_dwordx4 v[162:165], v[56:57], off nt
	s_nop 0
	global_load_dwordx4 v[166:169], v[58:59], off nt
	s_nop 0
	global_load_dwordx4 v[170:173], v[60:61], off nt
	s_nop 0
	global_load_dwordx4 v[174:177], v[62:63], off nt
	s_nop 0
	global_load_dwordx4 v[178:181], v[102:103], off nt
	global_load_dwordx4 v[182:185], v[104:105], off nt
	global_load_dwordx4 v[186:189], v[106:107], off nt
	global_load_dwordx4 v[190:193], v[108:109], off nt
	global_load_dwordx4 v[194:197], v[110:111], off nt
	global_load_dwordx4 v[198:201], v[112:113], off nt
	global_load_dwordx4 v[202:205], v[114:115], off nt
	global_load_dwordx4 v[206:209], v[116:117], off nt
	global_load_dwordx4 v[210:213], v[118:119], off nt
	global_load_dwordx4 v[214:217], v[120:121], off nt
	global_load_dwordx4 v[218:221], v[122:123], off nt
	global_load_dwordx4 v[222:225], v[124:125], off nt
	s_waitcnt vmcnt(15)
	ds_write2_b32 v14, v162, v163 offset1:1
	ds_write2_b32 v14, v164, v165 offset0:2 offset1:3
	s_waitcnt vmcnt(14)
	ds_write2_b32 v21, v166, v167 offset1:1
	ds_write2_b32 v22, v168, v169 offset1:1
	s_waitcnt vmcnt(13)
	ds_write2_b32 v23, v170, v171 offset1:1
	ds_write2_b32 v24, v172, v173 offset1:1
	s_waitcnt vmcnt(12)
	ds_write2_b32 v25, v174, v175 offset1:1
	ds_write2_b32 v26, v176, v177 offset1:1
	s_waitcnt vmcnt(11)
	ds_write2_b32 v27, v178, v179 offset1:1
	ds_write2_b32 v28, v180, v181 offset1:1
	s_waitcnt vmcnt(10)
	ds_write2_b32 v29, v182, v183 offset1:1
	ds_write2_b32 v30, v184, v185 offset1:1
	s_waitcnt vmcnt(9)
	ds_write2_b32 v31, v186, v187 offset1:1
	ds_write2_b32 v32, v188, v189 offset1:1
	s_waitcnt vmcnt(8)
	ds_write2_b32 v33, v190, v191 offset1:1
	ds_write2_b32 v34, v192, v193 offset1:1
	s_waitcnt vmcnt(7)
	ds_write2_b32 v35, v194, v195 offset1:1
	ds_write2_b32 v36, v196, v197 offset1:1
	s_waitcnt vmcnt(6)
	ds_write2_b32 v37, v198, v199 offset1:1
	ds_write2_b32 v38, v200, v201 offset1:1
	s_waitcnt vmcnt(5)
	ds_write2_b32 v39, v202, v203 offset1:1
	ds_write2_b32 v40, v204, v205 offset1:1
	s_waitcnt vmcnt(4)
	ds_write2_b32 v41, v206, v207 offset1:1
	ds_write2_b32 v42, v208, v209 offset1:1
	s_waitcnt vmcnt(3)
	ds_write2_b32 v43, v210, v211 offset1:1
	ds_write2_b32 v44, v212, v213 offset1:1
	s_waitcnt vmcnt(2)
	ds_write2_b32 v45, v214, v215 offset1:1
	ds_write2_b32 v46, v216, v217 offset1:1
	s_waitcnt vmcnt(1)
	ds_write2_b32 v47, v218, v219 offset1:1
	ds_write2_b32 v48, v220, v221 offset1:1
	s_waitcnt vmcnt(0)
	ds_write2_b32 v49, v222, v223 offset1:1
	ds_write2_b32 v50, v224, v225 offset1:1
	s_waitcnt lgkmcnt(0)
	ds_read2_b32 v[54:55], v13 offset0:65 offset1:73
	ds_read2_b32 v[56:57], v13 offset1:8
	ds_read2_b32 v[58:59], v13 offset0:130 offset1:138
	ds_read2_b32 v[60:61], v13 offset0:195 offset1:203
	ds_read2_b32 v[62:63], v52 offset0:4 offset1:12
	ds_read2_b32 v[64:65], v52 offset0:69 offset1:77
	ds_read2_b32 v[66:67], v52 offset0:134 offset1:142
	ds_read2_b32 v[68:69], v52 offset0:199 offset1:207
	ds_read2_b32 v[70:71], v13 offset0:81 offset1:89
	ds_read2_b32 v[72:73], v13 offset0:16 offset1:24
	ds_read2_b32 v[74:75], v13 offset0:146 offset1:154
	ds_read2_b32 v[76:77], v13 offset0:211 offset1:219
	ds_read2_b32 v[78:79], v52 offset0:20 offset1:28
	ds_read2_b32 v[80:81], v52 offset0:85 offset1:93
	ds_read2_b32 v[82:83], v52 offset0:150 offset1:158
	ds_read2_b32 v[84:85], v52 offset0:215 offset1:223
	ds_read2_b32 v[86:87], v13 offset0:32 offset1:40
	ds_read2_b32 v[88:89], v13 offset0:97 offset1:105
	ds_read2_b32 v[90:91], v13 offset0:162 offset1:170
	ds_read2_b32 v[92:93], v13 offset0:227 offset1:235
	ds_read2_b32 v[94:95], v52 offset0:36 offset1:44
	ds_read2_b32 v[96:97], v52 offset0:101 offset1:109
	ds_read2_b32 v[98:99], v52 offset0:166 offset1:174
	ds_read2_b32 v[100:101], v52 offset0:231 offset1:239
	ds_read2_b32 v[102:103], v13 offset0:48 offset1:56
	ds_read2_b32 v[104:105], v13 offset0:113 offset1:121
	ds_read2_b32 v[106:107], v13 offset0:178 offset1:186
	ds_read2_b32 v[108:109], v13 offset0:243 offset1:251
	ds_read2_b32 v[110:111], v52 offset0:52 offset1:60
	ds_read2_b32 v[112:113], v52 offset0:117 offset1:125
	ds_read2_b32 v[114:115], v52 offset0:182 offset1:190
	ds_read2_b32 v[116:117], v52 offset0:247 offset1:255
	s_waitcnt lgkmcnt(14)
	v_cvt_pk_bf16_f32 v8, v56, v54
	v_cvt_pk_bf16_f32 v9, v58, v60
	v_cvt_pk_bf16_f32 v10, v62, v64
	v_cvt_pk_bf16_f32 v11, v66, v68
	v_cvt_pk_bf16_f32 v54, v57, v55
	v_cvt_pk_bf16_f32 v55, v59, v61
	v_cvt_pk_bf16_f32 v56, v63, v65
	v_cvt_pk_bf16_f32 v57, v67, v69
	v_cvt_pk_bf16_f32 v58, v72, v70
	v_cvt_pk_bf16_f32 v59, v74, v76
	v_cvt_pk_bf16_f32 v60, v78, v80
	v_cvt_pk_bf16_f32 v61, v82, v84
	v_cvt_pk_bf16_f32 v62, v73, v71
	v_cvt_pk_bf16_f32 v63, v75, v77
	v_cvt_pk_bf16_f32 v64, v79, v81
	v_cvt_pk_bf16_f32 v65, v83, v85
	v_cvt_pk_bf16_f32 v66, v86, v88
	s_waitcnt lgkmcnt(12)
	v_cvt_pk_bf16_f32 v67, v90, v92
	v_cvt_pk_bf16_f32 v70, v87, v89
	v_cvt_pk_bf16_f32 v71, v91, v93
	s_waitcnt lgkmcnt(10)
	v_cvt_pk_bf16_f32 v68, v94, v96
	v_cvt_pk_bf16_f32 v72, v95, v97
	s_waitcnt lgkmcnt(8)
	v_cvt_pk_bf16_f32 v69, v98, v100
	v_cvt_pk_bf16_f32 v73, v99, v101
	s_waitcnt lgkmcnt(6)
	v_cvt_pk_bf16_f32 v74, v102, v104
	s_waitcnt lgkmcnt(4)
	v_cvt_pk_bf16_f32 v75, v106, v108
	v_cvt_pk_bf16_f32 v78, v103, v105
	v_cvt_pk_bf16_f32 v79, v107, v109
	s_waitcnt lgkmcnt(2)
	v_cvt_pk_bf16_f32 v76, v110, v112
	v_cvt_pk_bf16_f32 v80, v111, v113
	s_waitcnt lgkmcnt(0)
	v_cvt_pk_bf16_f32 v77, v114, v116
	v_cvt_pk_bf16_f32 v81, v115, v117
	global_store_dwordx4 v[126:127], v[8:11], off
	global_store_dwordx4 v[128:129], v[54:57], off
	global_store_dwordx4 v[132:133], v[58:61], off
	global_store_dwordx4 v[134:135], v[62:65], off
	global_store_dwordx4 v[136:137], v[66:69], off
	global_store_dwordx4 v[138:139], v[70:73], off
	global_store_dwordx4 v[140:141], v[74:77], off
	global_store_dwordx4 v[142:143], v[78:81], off
	v_add_u32_e32 v53, s14, v53
	s_waitcnt lgkmcnt(0)
	v_cmp_lt_i32_e32 vcc, s8, v53
	s_or_b64 s[6:7], vcc, s[6:7]
	s_andn2_b64 exec, exec, s[6:7]
	s_cbranch_execnz .LBB0_27
